# v23 + HGRN2 chunk loop instruction selection: 12 MFMA-adjacent packed f32 multiplies split, 24 scalar f32 pairs of the gate section packed (bit-identical)
# speedup vs baseline: 1.0080x; 1.0080x over previous
.LBB0_354:
	v_add_u32_e32 v8, 0x200, v8
	s_movk_i32 s70, 0x1fff
	v_cmp_lt_u32_e32 vcc, s70, v8
	ds_write_b32 v7, v69
	s_or_b64 s[58:59], vcc, s[58:59]
	v_add_u32_e32 v7, 0x800, v7
	s_andn2_b64 exec, exec, s[58:59]
	s_cbranch_execnz .LBB0_354
	s_or_b64 exec, exec, s[58:59]
	s_waitcnt vmcnt(0)
	v_sub_f32_e32 v4, v4, v2
	v_mul_f32_e32 v2, 0x3fb8aa3b, v4
	s_mov_b32 s46, 0x3fb8aa3b
	v_fma_f32 v7, v4, s46, -v2
	v_rndne_f32_e32 v8, v2
	v_fmac_f32_e32 v7, 0x32a5705f, v4
	v_sub_f32_e32 v2, v2, v8
	v_add_f32_e32 v2, v2, v7
	v_cvt_i32_f32_e32 v7, v8
	v_exp_f32_e32 v2, v2
	v_sub_f32_e32 v3, v5, v3
	s_and_b64 s[58:59], s[40:41], exec
	v_readlane_b32 s58, v254, 15
	v_ldexp_f32 v7, v2, v7
	v_mul_f32_e32 v2, 0x3fb8aa3b, v3
	v_fma_f32 v5, v3, s46, -v2
	v_rndne_f32_e32 v8, v2
	v_fmac_f32_e32 v5, 0x32a5705f, v3
	v_sub_f32_e32 v2, v2, v8
	v_add_f32_e32 v2, v2, v5
	v_exp_f32_e32 v5, v2
	v_cvt_i32_f32_e32 v8, v8
	s_mov_b32 s46, 0xc2ce8ed0
	v_cmp_ngt_f32_e32 vcc, s46, v4
	s_mov_b32 s89, 0x42b17218
	v_ldexp_f32 v5, v5, v8
	v_cndmask_b32_e32 v7, 0, v7, vcc
	v_cmp_ngt_f32_e32 vcc, s46, v3
	v_readlane_b32 s46, v254, 26
	s_cselect_b32 s58, s58, s46
	v_cndmask_b32_e32 v5, 0, v5, vcc
	v_cmp_nlt_f32_e32 vcc, s89, v3
	s_mulk_i32 s58, 0x1c00
	v_readlane_b32 s46, v254, 27
	v_cndmask_b32_e32 v3, v215, v5, vcc
	v_or_b32_e32 v5, s58, v6
	s_cselect_b32 s58, s60, s46
	s_mulk_i32 s58, 0x1c00
	v_readlane_b32 s46, v254, 28
	v_readlane_b32 s47, v254, 29
	v_or_b32_e32 v8, s58, v6
	s_cselect_b32 s58, s46, s47
	s_mulk_i32 s58, 0x1c00
	v_readlane_b32 s46, v254, 30
	v_readlane_b32 s47, v254, 31
	v_or_b32_e32 v9, s58, v6
	s_cselect_b32 s58, s46, s47
	s_mulk_i32 s58, 0x1c00
	v_readlane_b32 s46, v254, 32
	v_readlane_b32 s47, v254, 33
	v_or_b32_e32 v10, s58, v6
	s_cselect_b32 s58, s46, s47
	s_mulk_i32 s58, 0x1c00
	v_readlane_b32 s46, v254, 34
	v_readlane_b32 s47, v254, 35
	v_or_b32_e32 v11, s58, v6
	s_cselect_b32 s58, s46, s47
	s_mulk_i32 s58, 0x1c00
	v_readlane_b32 s46, v254, 36
	v_readlane_b32 s47, v254, 37
	v_or_b32_e32 v12, s58, v6
	s_cselect_b32 s58, s46, s47
	s_mulk_i32 s58, 0x1c00
	v_readlane_b32 s46, v254, 38
	v_readlane_b32 s47, v254, 39
	v_or_b32_e32 v13, s58, v6
	s_cselect_b32 s58, s46, s47
	s_mulk_i32 s58, 0x1c00
	v_add_f32_e32 v3, 1.0, v3
	v_or_b32_e32 v6, s58, v6
	v_lshlrev_b32_e32 v50, 1, v6
	v_div_scale_f32 v6, s[58:59], v3, v3, 1.0
	s_movk_i32 s58, 0x1800
	s_cselect_b32 s70, s58, 0x2000
	s_mov_b32 s58, 0x16600000
	s_cselect_b32 s58, s58, 0x1a600000
	s_add_u32 s82, s66, s58
	s_addc_u32 s83, s67, 0
	s_lshl_b32 s58, s5, 7
	s_and_b32 s88, s58, 0xfffff800
	s_and_b64 s[58:59], s[40:41], exec
	s_cselect_b32 s58, 0, 0x7c0
	s_or_b32 s58, s58, s88
	s_mul_hi_i32 s59, s58, 0x3800
	s_mulk_i32 s58, 0x3800
	s_add_u32 s86, s55, s58
	s_addc_u32 s87, s73, s59
	s_add_u32 s58, s86, s70
	s_addc_u32 s59, s87, 0
	s_add_u32 s84, s86, 0x1000
	s_addc_u32 s85, s87, 0
	v_lshlrev_b32_e32 v68, 1, v5
	s_add_u32 s86, s86, 0x2800
	v_lshlrev_b32_e32 v52, 1, v8
	v_lshlrev_b32_e32 v54, 1, v9
	v_lshlrev_b32_e32 v56, 1, v10
	v_lshlrev_b32_e32 v58, 1, v11
	v_lshlrev_b32_e32 v60, 1, v12
	v_lshlrev_b32_e32 v62, 1, v13
	s_addc_u32 s87, s87, 0
	global_load_dword v87, v68, s[58:59]
	global_load_dword v89, v68, s[84:85]
	global_load_dword v91, v68, s[86:87]
	global_load_dword v93, v52, s[58:59]
	global_load_dword v97, v52, s[84:85]
	global_load_dword v107, v52, s[86:87]
	global_load_dword v147, v54, s[84:85]
	global_load_dword v148, v54, s[86:87]
	global_load_dword v146, v54, s[58:59]
	global_load_dword v149, v56, s[58:59]
	global_load_dword v150, v56, s[84:85]
	global_load_dword v151, v56, s[86:87]
	global_load_dword v152, v58, s[58:59]
	global_load_dword v153, v58, s[84:85]
	global_load_dword v154, v58, s[86:87]
	global_load_dword v157, v60, s[86:87]
	global_load_dword v155, v60, s[58:59]
	global_load_dword v156, v60, s[84:85]
	global_load_dword v158, v62, s[58:59]
	global_load_dword v159, v62, s[84:85]
	global_load_dword v160, v62, s[86:87]
	global_load_dword v161, v50, s[58:59]
	global_load_dword v164, v50, s[84:85]
	global_load_dword v165, v50, s[86:87]
	v_rcp_f32_e32 v14, v6
	v_cmp_nlt_f32_e32 vcc, s89, v4
	v_readlane_b32 s46, v254, 40
	s_waitcnt lgkmcnt(0)
	v_fma_f32 v5, -v6, v14, 1.0
	v_cndmask_b32_e32 v4, v215, v7, vcc
	v_fmac_f32_e32 v14, v5, v14
	v_div_scale_f32 v5, vcc, 1.0, v3, 1.0
	v_mul_f32_e32 v7, v5, v14
	v_fma_f32 v8, -v6, v7, v5
	v_fmac_f32_e32 v7, v8, v14
	v_fma_f32 v5, -v6, v7, v5
	v_add_f32_e32 v4, 1.0, v4
	v_div_fmas_f32 v5, v5, v14, v7
	v_div_fixup_f32 v65, v5, v3, 1.0
	v_div_scale_f32 v3, s[58:59], v4, v4, 1.0
	v_rcp_f32_e32 v5, v3
	v_or_b32_e32 v6, s61, v189
	v_lshlrev_b32_e32 v6, 1, v6
	s_barrier
	v_fma_f32 v7, -v3, v5, 1.0
	v_fmac_f32_e32 v5, v7, v5
	v_div_scale_f32 v7, vcc, 1.0, v4, 1.0
	v_mul_f32_e32 v8, v7, v5
	v_fma_f32 v9, -v3, v8, v7
	v_fmac_f32_e32 v8, v9, v5
	v_fma_f32 v3, -v3, v8, v7
	v_div_fmas_f32 v3, v3, v5, v8
	v_div_fixup_f32 v64, v3, v4, 1.0
	v_cndmask_b32_e64 v3, v188, v187, s[40:41]
	v_lshlrev_b32_e32 v3, 11, v3
	v_mov_b32_e32 v2, 0
	v_or3_b32 v4, v6, s46, v3
	v_mov_b32_e32 v5, v69
	s_mov_b32 s89, 0
	v_pk_add_f32 v[108:109], v[64:65], 1.0 op_sel_hi:[1,0] neg_lo:[1,0] neg_hi:[1,0]
	v_mov_b32_e32 v53, v69
	v_mov_b32_e32 v55, v69
	v_mov_b32_e32 v57, v69
	v_mov_b32_e32 v59, v69
	v_mov_b32_e32 v61, v69
	v_mov_b32_e32 v63, v69
	v_mov_b32_e32 v51, v69
	v_lshl_add_u64 v[110:111], s[82:83], 0, v[4:5]
	s_movk_i32 s90, 0x780
	s_mov_b32 s91, 0
	v_mov_b32_e32 v3, v2
	v_mov_b32_e32 v4, v2
	v_mov_b32_e32 v5, v2
	v_mov_b32_e32 v6, v2
	v_mov_b32_e32 v7, v2
	v_mov_b32_e32 v8, v2
	v_mov_b32_e32 v9, v2
	v_mov_b32_e32 v10, v2
	v_mov_b32_e32 v11, v2
	v_mov_b32_e32 v12, v2
	v_mov_b32_e32 v13, v2
	v_mov_b32_e32 v14, v2
	v_mov_b32_e32 v15, v2
	v_mov_b32_e32 v16, v2
	v_mov_b32_e32 v17, v2
	v_mov_b32_e32 v18, v2
	v_mov_b32_e32 v19, v2
	v_mov_b32_e32 v20, v2
	v_mov_b32_e32 v21, v2
	v_mov_b32_e32 v22, v2
	v_mov_b32_e32 v23, v2
	v_mov_b32_e32 v24, v2
	v_mov_b32_e32 v25, v2
	v_mov_b32_e32 v26, v2
	v_mov_b32_e32 v27, v2
	v_mov_b32_e32 v28, v2
	v_mov_b32_e32 v29, v2
	v_mov_b32_e32 v30, v2
	v_mov_b32_e32 v31, v2
	v_mov_b32_e32 v32, v2
	v_mov_b32_e32 v33, v2
	s_mov_b32 s92, 0xbfb8aa3b
	s_mov_b32 s93, 0xbfb8aa3b
	s_branch .LBB0_357
.LBB0_356:
	s_nop 6
	v_cndmask_b32_e64 v34, v34, 0, s[30:31]
	v_cndmask_b32_e64 v35, 0, v35, s[34:35]
	v_cvt_pk_bf16_f32 v34, v34, v35
	v_cndmask_b32_e64 v35, v36, 0, s[36:37]
	v_cndmask_b32_e64 v36, v37, 0, s[38:39]
	v_cvt_pk_bf16_f32 v35, v35, v36
	ds_write_b64 v208, v[34:35]
	s_waitcnt lgkmcnt(0)
	s_barrier
	ds_read_b128 v[34:37], v209 offset:53248
	ds_read_b128 v[42:45], v209 offset:53312
	v_add_u32_e32 v38, v193, v182
	ds_read_b128 v[46:49], v38
	ds_read_b128 v[112:115], v38 offset:64
	s_bitcmp0_b32 s91, 0
	s_waitcnt lgkmcnt(1)
	v_mfma_f32_16x16x32_bf16 v[34:37], v[34:37], v[46:49], 0
	s_cselect_b32 s58, 0x13c00, s4
	v_add3_u32 v144, v183, s58, v195
	ds_read_b128 v[116:119], v144
	ds_read_b128 v[38:41], v216
	s_waitcnt lgkmcnt(2)
	v_mfma_f32_16x16x32_bf16 v[42:45], v[42:45], v[112:115], v[34:37]
	ds_read_b128 v[120:123], v144 offset:64
	s_nop 1
	ds_read_b128 v[34:37], v216 offset:64
	ds_read_b128 v[124:127], v212 offset:53312
	s_cselect_b32 s58, s4, 0x13c00
	v_add_u32_e32 v170, s58, v194
	s_waitcnt lgkmcnt(3)
	v_mfma_f32_16x16x32_bf16 v[42:45], v[116:119], v[38:41], v[42:45]
	ds_read_b128 v[116:119], v144 offset:128
	ds_read_b128 v[128:131], v216 offset:128
	s_add_i32 s61, s90, 64
	s_and_b64 s[58:59], s[40:41], exec
	s_waitcnt lgkmcnt(3)
	v_mfma_f32_16x16x32_bf16 v[120:123], v[120:123], v[34:37], v[42:45]
	ds_read_b128 v[132:135], v144 offset:192
	s_nop 1
	ds_read_b128 v[42:45], v216 offset:192
	ds_read_b128 v[136:139], v144 offset:4352
	s_cselect_b32 s58, s89, s61
	s_waitcnt lgkmcnt(3)
	v_mfma_f32_16x16x32_bf16 v[116:119], v[116:119], v[128:131], v[120:123]
	s_or_b32 s58, s58, s88
	s_ashr_i32 s59, s58, 31
	s_lshl_b64 s[58:59], s[58:59], 11
	ds_read_b128 v[120:123], v209 offset:55552
	s_waitcnt lgkmcnt(2)
	v_mfma_f32_16x16x32_bf16 v[116:119], v[132:135], v[42:45], v[116:119]
	ds_read_b128 v[132:135], v209 offset:55616
	s_add_i32 s89, s89, 64
	s_sub_i32 s90, s90, 64
	s_waitcnt lgkmcnt(1)
	v_mfma_f32_16x16x32_bf16 v[120:123], v[120:123], v[46:49], 0
	s_add_i32 s91, s91, 1
	s_cmpk_eq_i32 s90, 0xff80
	s_waitcnt lgkmcnt(0)
	v_mfma_f32_16x16x32_bf16 v[120:123], v[132:135], v[112:115], v[120:123]
	ds_read_b128 v[132:135], v144 offset:4416
	v_mfma_f32_16x16x32_bf16 v[120:123], v[136:139], v[38:41], v[120:123]
	ds_read_b128 v[136:139], v144 offset:4480
	s_waitcnt lgkmcnt(1)
	v_mfma_f32_16x16x32_bf16 v[120:123], v[132:135], v[34:37], v[120:123]
	ds_read_b128 v[132:135], v144 offset:4544
	s_waitcnt lgkmcnt(1)
	v_mfma_f32_16x16x32_bf16 v[120:123], v[136:139], v[128:131], v[120:123]
	ds_read_b128 v[136:139], v209 offset:57856
	s_waitcnt lgkmcnt(1)
	v_mfma_f32_16x16x32_bf16 v[120:123], v[132:135], v[42:45], v[120:123]
	ds_read_b128 v[132:135], v209 offset:57920
	ds_read_b128 v[140:143], v144 offset:8704
	ds_read_b128 v[166:169], v144 offset:8768
	ds_read_b128 v[218:221], v144 offset:8832
	ds_read_b128 v[222:225], v144 offset:8896
	s_waitcnt lgkmcnt(5)
	v_mfma_f32_16x16x32_bf16 v[136:139], v[136:139], v[46:49], 0
	s_waitcnt lgkmcnt(4)
	v_mfma_f32_16x16x32_bf16 v[132:135], v[132:135], v[112:115], v[136:139]
	s_nop 5
	ds_read_b128 v[136:139], v210
	ds_read_b128 v[226:229], v211 offset:34816
	ds_read_b128 v[230:233], v209 offset:60160
	ds_read_b128 v[234:237], v209 offset:60224
	s_waitcnt lgkmcnt(3)
	v_mul_f32_e32 v2, v2, v136
	v_mul_f32_e32 v3, v3, v137
	v_mfma_f32_16x16x32_bf16 v[132:135], v[140:143], v[38:41], v[132:135]
	ds_read_b128 v[140:143], v211 offset:34880
	ds_read_b128 v[238:241], v212 offset:53248
	ds_read_b128 v[242:245], v144 offset:13056
	ds_read_b128 v[246:249], v144 offset:13120
	v_mul_f32_e32 v4, v4, v138
	v_mul_f32_e32 v5, v5, v139
	v_mul_f32_e32 v6, v6, v136
	v_mul_f32_e32 v7, v7, v137
	v_mfma_f32_16x16x32_bf16 v[132:135], v[166:169], v[34:37], v[132:135]
	v_mul_f32_e64 v8, v8, v138
	v_mul_f32_e64 v9, v9, v139
	v_mul_f32_e32 v10, v10, v136
	v_mul_f32_e32 v11, v11, v137
	v_mul_f32_e32 v12, v12, v138
	v_mul_f32_e32 v13, v13, v139
	s_waitcnt lgkmcnt(2)
	v_mfma_f32_16x16x32_bf16 v[2:5], v[226:229], v[238:241], v[2:5]
	ds_read_b128 v[238:241], v144 offset:13184
	ds_read_b128 v[250:253], v144 offset:13248
	v_mul_f32_e32 v14, v14, v136
	v_mul_f32_e32 v15, v15, v137
	v_mul_f32_e32 v16, v16, v138
	v_mul_f32_e32 v17, v17, v139
	v_mfma_f32_16x16x32_bf16 v[2:5], v[140:143], v[124:127], v[2:5]
	v_add_u32_e32 v126, v170, v184
	v_add_u32_e32 v170, v170, v196
	v_mul_f32_e32 v18, v18, v136
	v_mul_f32_e32 v19, v19, v137
	v_mfma_f32_16x16x32_bf16 v[46:49], v[230:233], v[46:49], 0
	v_mul_f32_e64 v20, v20, v138
	v_mul_f32_e64 v21, v21, v139
	s_nop 1
	v_cvt_pk_bf16_f32 v124, v2, v3
	v_cvt_pk_bf16_f32 v125, v4, v5
	ds_write_b64 v126, v[124:125]
	ds_read_b128 v[124:127], v212 offset:55552
	ds_read_b128 v[166:169], v212 offset:55616
	s_waitcnt lgkmcnt(1)
	v_mfma_f32_16x16x32_bf16 v[6:9], v[226:229], v[124:127], v[6:9]
	v_mul_f32_e64 v22, v22, v136
	v_mul_f32_e64 v23, v23, v137
	v_mul_f32_e32 v24, v24, v138
	v_mul_f32_e32 v25, v25, v139
	v_mul_f32_e32 v26, v26, v136
	v_mul_f32_e32 v27, v27, v137
	s_waitcnt lgkmcnt(0)
	v_mfma_f32_16x16x32_bf16 v[6:9], v[140:143], v[166:169], v[6:9]
	v_mul_f32_e64 v28, v28, v138
	v_mul_f32_e64 v29, v29, v139
	v_mul_f32_e32 v30, v30, v136
	v_mul_f32_e32 v31, v31, v137
	v_mul_f32_e32 v32, v32, v138
	v_mul_f32_e32 v33, v33, v139
	v_mfma_f32_16x16x32_bf16 v[124:127], v[218:221], v[128:131], v[132:135]
	v_mfma_f32_16x16x32_bf16 v[46:49], v[234:237], v[112:115], v[46:49]
	s_nop 1
	v_cvt_pk_bf16_f32 v144, v6, v7
	v_cvt_pk_bf16_f32 v145, v8, v9
	ds_write_b64 v170, v[144:145]
	ds_read_b128 v[132:135], v212 offset:57856
	ds_read_b128 v[166:169], v212 offset:57920
	s_waitcnt lgkmcnt(1)
	v_mfma_f32_16x16x32_bf16 v[10:13], v[226:229], v[132:135], v[10:13]
	s_waitcnt lgkmcnt(0)
	v_mfma_f32_16x16x32_bf16 v[10:13], v[140:143], v[166:169], v[10:13]
	v_mfma_f32_16x16x32_bf16 v[38:41], v[242:245], v[38:41], v[46:49]
	v_mfma_f32_16x16x32_bf16 v[34:37], v[246:249], v[34:37], v[38:41]
	s_nop 5
	v_cvt_pk_bf16_f32 v132, v10, v11
	v_cvt_pk_bf16_f32 v133, v12, v13
	ds_write_b64 v170, v[132:133] offset:4352
	ds_read_b128 v[132:135], v212 offset:60160
	ds_read_b128 v[112:115], v212 offset:60224
	s_waitcnt lgkmcnt(1)
	v_mfma_f32_16x16x32_bf16 v[14:17], v[226:229], v[132:135], v[14:17]
	v_lshl_add_u64 v[132:133], v[110:111], 0, s[58:59]
	s_waitcnt lgkmcnt(0)
	v_mfma_f32_16x16x32_bf16 v[14:17], v[140:143], v[112:115], v[14:17]
	v_mfma_f32_16x16x32_bf16 v[124:127], v[222:225], v[42:45], v[124:127]
	v_mfma_f32_16x16x32_bf16 v[34:37], v[238:241], v[128:131], v[34:37]
	s_nop 5
	v_cvt_pk_bf16_f32 v112, v14, v15
	v_cvt_pk_bf16_f32 v113, v16, v17
	ds_write_b64 v170, v[112:113] offset:8704
	ds_read_b128 v[112:115], v212 offset:62464
	ds_read_b128 v[46:49], v212 offset:62528
	s_waitcnt lgkmcnt(1)
	v_mfma_f32_16x16x32_bf16 v[18:21], v[226:229], v[112:115], v[18:21]
	v_cvt_pk_bf16_f32 v112, v116, v117
	v_cvt_pk_bf16_f32 v113, v118, v119
	global_store_dwordx2 v[132:133], v[112:113], off
	s_waitcnt lgkmcnt(0)
	v_mfma_f32_16x16x32_bf16 v[18:21], v[140:143], v[46:49], v[18:21]
	v_mfma_f32_16x16x32_bf16 v[34:37], v[250:253], v[42:45], v[34:37]
	s_nop 6
	v_cvt_pk_bf16_f32 v46, v18, v19
	v_cvt_pk_bf16_f32 v47, v20, v21
	ds_write_b64 v170, v[46:47] offset:13056
	ds_read_b128 v[46:49], v212 offset:64768
	ds_read_b128 v[38:41], v212 offset:64832
	s_waitcnt lgkmcnt(1)
	v_mfma_f32_16x16x32_bf16 v[22:25], v[226:229], v[46:49], v[22:25]
	v_cvt_pk_bf16_f32 v46, v120, v121
	v_cvt_pk_bf16_f32 v47, v122, v123
	global_store_dwordx2 v[132:133], v[46:47], off offset:32
	s_waitcnt lgkmcnt(0)
	v_mfma_f32_16x16x32_bf16 v[22:25], v[140:143], v[38:41], v[22:25]
	v_cvt_pk_bf16_f32 v34, v34, v35
	v_cvt_pk_bf16_f32 v35, v36, v37
	global_store_dwordx2 v[132:133], v[34:35], off offset:96
	s_nop 4
	v_cvt_pk_bf16_f32 v38, v22, v23
	v_cvt_pk_bf16_f32 v39, v24, v25
	ds_write_b64 v170, v[38:39] offset:17408
	ds_read_b128 v[38:41], v213 offset:62464
	ds_read_b128 v[46:49], v213 offset:62528
	s_waitcnt lgkmcnt(1)
	v_mfma_f32_16x16x32_bf16 v[26:29], v[226:229], v[38:41], v[26:29]
	v_cvt_pk_bf16_f32 v38, v124, v125
	v_cvt_pk_bf16_f32 v39, v126, v127
	global_store_dwordx2 v[132:133], v[38:39], off offset:64
	s_waitcnt lgkmcnt(0)
	v_mfma_f32_16x16x32_bf16 v[26:29], v[140:143], v[46:49], v[26:29]
	s_nop 7
	v_cvt_pk_bf16_f32 v38, v26, v27
	v_cvt_pk_bf16_f32 v39, v28, v29
	ds_write_b64 v170, v[38:39] offset:21760
	ds_read_b128 v[38:41], v213 offset:64768
	ds_read_b128 v[42:45], v213 offset:64832
	s_waitcnt lgkmcnt(1)
	v_mfma_f32_16x16x32_bf16 v[30:33], v[226:229], v[38:41], v[30:33]
	s_waitcnt lgkmcnt(0)
	v_mfma_f32_16x16x32_bf16 v[30:33], v[140:143], v[42:45], v[30:33]
	s_nop 7
	v_cvt_pk_bf16_f32 v34, v30, v31
	v_cvt_pk_bf16_f32 v35, v32, v33
	ds_write_b64 v170, v[34:35] offset:26112
	s_waitcnt lgkmcnt(0)
	s_barrier
	s_cbranch_scc1 .LBB0_313
.LBB0_357:
	s_waitcnt vmcnt(23)
	v_lshlrev_b32_e32 v34, 16, v87
	v_and_b32_e32 v35, 0xffff0000, v87
	v_mul_f32_e32 v34, 0xbfb8aa3b, v34
	v_mul_f32_e32 v35, 0xbfb8aa3b, v35
	v_exp_f32_e32 v34, v34
	v_exp_f32_e32 v35, v35
	s_waitcnt vmcnt(20)
	v_lshlrev_b32_e32 v36, 16, v93
	v_add_u32_e32 v167, 0, v190
	v_add_f32_e32 v34, 1.0, v34
	v_add_f32_e32 v35, 1.0, v35
	v_rcp_f32_e32 v34, v34
	v_rcp_f32_e32 v35, v35
	s_andn2_b64 vcc, exec, s[74:75]
	s_mov_b64 s[58:59], -1
	v_pk_mul_f32 v[120:121], v[108:109], v[34:35]
	v_and_b32_e32 v34, 0xffff0000, v93
	v_mul_f32_e32 v35, 0xbfb8aa3b, v36
	v_mul_f32_e32 v34, 0xbfb8aa3b, v34
	v_exp_f32_e32 v35, v35
	v_exp_f32_e32 v36, v34
	v_add_f32_e32 v37, v64, v120
	v_add_f32_e32 v38, v65, v121
	v_add_f32_e32 v34, 1.0, v35
	v_add_f32_e32 v35, 1.0, v36
	v_rcp_f32_e32 v34, v34
	v_rcp_f32_e32 v35, v35
	v_log_f32_e32 v36, v37
	v_log_f32_e32 v37, v38
	v_pk_mul_f32 v[122:123], v[108:109], v[34:35]
	s_waitcnt vmcnt(15)
	v_lshlrev_b32_e32 v34, 16, v146
	v_and_b32_e32 v35, 0xffff0000, v146
	v_pk_mul_f32 v[34:35], v[34:35], s[92:93]
	v_exp_f32_e32 v34, v34
	v_exp_f32_e32 v35, v35
	v_pk_add_f32 v[38:39], v[64:65], v[122:123]
	v_pk_add_f32 v[34:35], v[34:35], 1.0 op_sel_hi:[1,0]
	v_rcp_f32_e32 v34, v34
	v_rcp_f32_e32 v35, v35
	v_log_f32_e32 v38, v38
	v_log_f32_e32 v39, v39
	v_pk_add_f32 v[144:145], v[36:37], 0 op_sel_hi:[1,0]
	v_pk_mul_f32 v[128:129], v[108:109], v[34:35]
	s_waitcnt vmcnt(14)
	v_lshlrev_b32_e32 v34, 16, v149
	v_and_b32_e32 v35, 0xffff0000, v149
	v_pk_mul_f32 v[34:35], v[34:35], s[92:93]
	v_exp_f32_e32 v34, v34
	v_exp_f32_e32 v35, v35
	v_pk_add_f32 v[40:41], v[64:65], v[128:129]
	v_pk_add_f32 v[34:35], v[34:35], 1.0 op_sel_hi:[1,0]
	v_rcp_f32_e32 v34, v34
	v_rcp_f32_e32 v35, v35
	v_log_f32_e32 v40, v40
	v_log_f32_e32 v41, v41
	v_pk_add_f32 v[140:141], v[144:145], v[38:39]
	v_pk_mul_f32 v[126:127], v[108:109], v[34:35]
	s_waitcnt vmcnt(11)
	v_lshlrev_b32_e32 v34, 16, v152
	v_and_b32_e32 v35, 0xffff0000, v152
	v_pk_mul_f32 v[34:35], v[34:35], s[92:93]
	v_exp_f32_e32 v34, v34
	v_exp_f32_e32 v35, v35
	v_pk_add_f32 v[42:43], v[64:65], v[126:127]
	v_pk_add_f32 v[34:35], v[34:35], 1.0 op_sel_hi:[1,0]
	v_rcp_f32_e32 v34, v34
	v_rcp_f32_e32 v35, v35
	v_log_f32_e32 v42, v42
	v_log_f32_e32 v43, v43
	v_pk_add_f32 v[136:137], v[140:141], v[40:41]
	v_pk_mul_f32 v[130:131], v[108:109], v[34:35]
	s_waitcnt vmcnt(7)
	v_lshlrev_b32_e32 v34, 16, v155
	v_and_b32_e32 v35, 0xffff0000, v155
	v_pk_mul_f32 v[34:35], v[34:35], s[92:93]
	v_exp_f32_e32 v34, v34
	v_exp_f32_e32 v35, v35
	v_pk_add_f32 v[44:45], v[64:65], v[130:131]
	v_pk_add_f32 v[34:35], v[34:35], 1.0 op_sel_hi:[1,0]
	v_rcp_f32_e32 v34, v34
	v_rcp_f32_e32 v35, v35
	v_log_f32_e32 v44, v44
	v_log_f32_e32 v45, v45
	v_pk_add_f32 v[132:133], v[136:137], v[42:43]
	v_pk_mul_f32 v[134:135], v[108:109], v[34:35]
	s_waitcnt vmcnt(5)
	v_lshlrev_b32_e32 v34, 16, v158
	v_and_b32_e32 v35, 0xffff0000, v158
	v_pk_mul_f32 v[34:35], v[34:35], s[92:93]
	v_exp_f32_e32 v34, v34
	v_exp_f32_e32 v35, v35
	v_pk_add_f32 v[46:47], v[64:65], v[134:135]
	v_pk_add_f32 v[34:35], v[34:35], 1.0 op_sel_hi:[1,0]
	v_rcp_f32_e32 v34, v34
	v_rcp_f32_e32 v35, v35
	v_log_f32_e32 v46, v46
	v_log_f32_e32 v47, v47
	v_pk_add_f32 v[124:125], v[132:133], v[44:45]
	v_pk_mul_f32 v[138:139], v[108:109], v[34:35]
	s_waitcnt vmcnt(2)
	v_lshlrev_b32_e32 v34, 16, v161
	v_and_b32_e32 v35, 0xffff0000, v161
	v_pk_mul_f32 v[34:35], v[34:35], s[92:93]
	v_exp_f32_e32 v34, v34
	v_exp_f32_e32 v35, v35
	v_pk_add_f32 v[48:49], v[64:65], v[138:139]
	v_pk_add_f32 v[34:35], v[34:35], 1.0 op_sel_hi:[1,0]
	v_rcp_f32_e32 v34, v34
	v_rcp_f32_e32 v35, v35
	v_log_f32_e32 v48, v48
	v_log_f32_e32 v49, v49
	v_pk_add_f32 v[118:119], v[124:125], v[46:47]
	v_pk_mul_f32 v[142:143], v[108:109], v[34:35]
	v_and_b32_e32 v36, 0xffff, v154
	v_pk_add_f32 v[34:35], v[64:65], v[142:143]
	v_log_f32_e32 v34, v34
	v_log_f32_e32 v35, v35
	v_pk_add_f32 v[114:115], v[118:119], v[48:49]
	v_and_b32_e32 v37, 0xffff, v160
	v_lshl_or_b32 v36, v157, 16, v36
	v_pk_add_f32 v[112:113], v[114:115], v[34:35]
	v_add_u32_e32 v34, s63, v190
	ds_write_b64 v34, v[112:113]
	v_and_b32_e32 v34, 0xffff, v91
	v_and_b32_e32 v35, 0xffff, v148
	v_lshl_or_b32 v34, v107, 16, v34
	v_lshl_or_b32 v35, v151, 16, v35
	s_waitcnt vmcnt(0)
	v_lshl_or_b32 v37, v165, 16, v37
	v_lshrrev_b32_e32 v38, 16, v91
	v_lshrrev_b32_e32 v39, 16, v148
	v_lshrrev_b32_e32 v40, 16, v154
	v_lshrrev_b32_e32 v41, 16, v160
	v_add_u32_e32 v42, s64, v191
	v_and_or_b32 v38, v107, s53, v38
	v_and_or_b32 v39, v151, s53, v39
	v_and_or_b32 v40, v157, s53, v40
	v_and_or_b32 v41, v165, s53, v41
	ds_write_b128 v42, v[34:37] offset:53248
	ds_write_b128 v42, v[38:41] offset:53392
	s_waitcnt lgkmcnt(0)
	s_barrier
	v_add_u32_e32 v34, 0x24c00, v167
	ds_read2st64_b64 v[46:49], v34 offset1:1
	ds_read2st64_b64 v[42:45], v34 offset0:2 offset1:3
	ds_read2st64_b64 v[38:41], v34 offset0:4 offset1:5
	ds_read2st64_b64 v[34:37], v34 offset0:6 offset1:7
	s_waitcnt lgkmcnt(3)
	v_add_f32_e32 v166, 0, v46
	v_add_f32_e32 v46, v166, v48
	s_waitcnt lgkmcnt(2)
	v_add_f32_e32 v46, v46, v42
	v_add_f32_e32 v46, v46, v44
	s_waitcnt lgkmcnt(1)
	v_add_f32_e32 v46, v46, v38
	v_add_f32_e32 v46, v46, v40
	s_waitcnt lgkmcnt(0)
	v_add_f32_e32 v46, v46, v34
	v_add_f32_e32 v46, v46, v36
	v_exp_f32_e32 v116, v46
	s_cbranch_vccnz .LBB0_359
	s_mov_b64 s[58:59], 0

.LBB0_361:
	v_cndmask_b32_e64 v47, v47, 0, s[44:45]
	v_cndmask_b32_e64 v166, v166, 0, s[44:45]
	v_add_f32_e32 v48, v48, v166
	v_add_f32_e32 v49, v49, v47
	v_cndmask_b32_e64 v47, v47, v49, s[8:9]
	v_cndmask_b32_e64 v48, v166, v48, s[8:9]
	v_add_f32_e32 v42, v42, v48
	v_add_f32_e32 v43, v43, v47
	v_cndmask_b32_e64 v43, v47, v43, s[10:11]
	v_cndmask_b32_e64 v42, v48, v42, s[10:11]
	v_pk_add_f32 v[44:45], v[44:45], v[42:43]
	v_cndmask_b32_e64 v43, v43, v45, s[12:13]
	v_cndmask_b32_e64 v42, v42, v44, s[12:13]
	v_pk_add_f32 v[38:39], v[38:39], v[42:43]
	v_cndmask_b32_e64 v39, v43, v39, s[14:15]
	v_cndmask_b32_e64 v38, v42, v38, s[14:15]
	v_pk_add_f32 v[40:41], v[40:41], v[38:39]
	v_cndmask_b32_e64 v39, v39, v41, s[16:17]
	v_cndmask_b32_e64 v38, v38, v40, s[16:17]
	v_pk_add_f32 v[34:35], v[34:35], v[38:39]
	v_cndmask_b32_e64 v35, v39, v35, s[18:19]
	v_cndmask_b32_e64 v34, v38, v34, s[18:19]
	v_pk_add_f32 v[36:37], v[36:37], v[34:35]
	v_cndmask_b32_e64 v47, v35, v37, s[20:21]
	v_cndmask_b32_e64 v166, v34, v36, s[20:21]
	v_add_f32_e32 v34, v144, v166
	v_add_f32_e32 v35, v145, v47
	v_exp_f32_e32 v34, v34
	v_exp_f32_e32 v35, v35
	v_pk_add_f32 v[120:121], v[108:109], v[120:121] neg_lo:[0,1] neg_hi:[0,1]
	v_pk_add_f32 v[36:37], v[108:109], v[126:127] neg_lo:[0,1] neg_hi:[0,1]
	v_rcp_f32_e32 v40, v34
	v_rcp_f32_e32 v41, v35
	v_add_f32_e32 v126, v140, v166
	v_add_f32_e32 v127, v141, v47
	v_exp_f32_e32 v126, v126
	v_pk_mul_f32 v[40:41], v[120:121], v[40:41]
	v_lshlrev_b32_e32 v120, 16, v89
	v_and_b32_e32 v121, 0xffff0000, v89
	v_exp_f32_e32 v127, v127
	v_pk_mul_f32 v[34:35], v[34:35], v[120:121]
	s_mul_i32 s58, s57, 0x880
	v_pk_add_f32 v[38:39], v[108:109], v[130:131] neg_lo:[0,1] neg_hi:[0,1]
	v_cvt_pk_bf16_f32 v120, v34, v35
	v_add_u32_e32 v121, s58, v192
	v_cvt_pk_bf16_f32 v130, v40, v41
	ds_write2st64_b32 v121, v120, v130 offset1:68
	v_lshlrev_b32_e32 v120, 16, v97
	v_and_b32_e32 v121, 0xffff0000, v97
	v_pk_mul_f32 v[120:121], v[126:127], v[120:121]
	v_rcp_f32_e32 v34, v126
	v_cvt_pk_bf16_f32 v130, v120, v121
	v_add_f32_e32 v120, v136, v166
	v_add_f32_e32 v121, v137, v47
	v_exp_f32_e32 v120, v120
	v_exp_f32_e32 v121, v121
	v_rcp_f32_e32 v35, v127
	v_pk_add_f32 v[122:123], v[108:109], v[122:123] neg_lo:[0,1] neg_hi:[0,1]
	v_rcp_f32_e32 v126, v120
	v_rcp_f32_e32 v127, v121
	v_pk_mul_f32 v[34:35], v[122:123], v[34:35]
	v_pk_add_f32 v[128:129], v[108:109], v[128:129] neg_lo:[0,1] neg_hi:[0,1]
	v_pk_add_f32 v[42:43], v[108:109], v[134:135] neg_lo:[0,1] neg_hi:[0,1]
	v_cvt_pk_bf16_f32 v134, v34, v35
	v_mov_b32_e32 v123, v34
	v_mov_b32_e32 v34, v41
	v_mov_b32_e32 v122, v40
	v_pk_mul_f32 v[40:41], v[46:47], v[34:35] op_sel_hi:[0,1]
	v_pk_mul_f32 v[34:35], v[128:129], v[126:127]
	v_lshlrev_b32_e32 v126, 16, v147
	v_and_b32_e32 v127, 0xffff0000, v147
	v_pk_mul_f32 v[120:121], v[120:121], v[126:127]
	v_add_f32_e32 v126, v132, v166
	v_add_f32_e32 v127, v133, v47
	v_exp_f32_e32 v126, v126
	v_exp_f32_e32 v127, v127
	s_mul_i32 s58, s60, 0x110
	v_add_u32_e32 v131, s58, v192
	v_cvt_pk_bf16_f32 v120, v120, v121
	ds_write2_b32 v131, v130, v120 offset1:68
	v_rcp_f32_e32 v120, v126
	v_rcp_f32_e32 v121, v127
	v_cvt_pk_bf16_f32 v128, v34, v35
	v_add_u32_e32 v130, 0x4400, v131
	ds_write2_b32 v130, v134, v128 offset1:68
	v_pk_mul_f32 v[36:37], v[36:37], v[120:121]
	v_lshlrev_b32_e32 v120, 16, v150
	v_and_b32_e32 v121, 0xffff0000, v150
	v_pk_mul_f32 v[120:121], v[126:127], v[120:121]
	v_cvt_pk_bf16_f32 v133, v36, v37
	v_cvt_pk_bf16_f32 v132, v120, v121
	v_add_f32_e32 v120, v124, v166
	v_add_f32_e32 v121, v125, v47
	v_exp_f32_e32 v120, v120
	v_exp_f32_e32 v121, v121
	v_mov_b32_e32 v124, v34
	v_mov_b32_e32 v125, v36
	v_rcp_f32_e32 v126, v120
	v_rcp_f32_e32 v127, v121
	v_mov_b32_e32 v36, v35
	v_pk_mul_f32 v[128:129], v[46:47], v[36:37] op_sel_hi:[0,1]
	v_lshlrev_b32_e32 v36, 16, v153
	v_pk_mul_f32 v[34:35], v[38:39], v[126:127]
	v_add_f32_e32 v38, v118, v166
	v_add_f32_e32 v39, v119, v47
	v_exp_f32_e32 v38, v38
	v_exp_f32_e32 v39, v39
	v_and_b32_e32 v37, 0xffff0000, v153
	v_pk_mul_f32 v[36:37], v[120:121], v[36:37]
	v_pk_add_f32 v[44:45], v[108:109], v[138:139] neg_lo:[0,1] neg_hi:[0,1]
	v_cvt_pk_bf16_f32 v118, v36, v37
	v_rcp_f32_e32 v36, v38
	v_rcp_f32_e32 v37, v39
	ds_write2_b32 v131, v132, v118 offset0:136 offset1:204
	v_cvt_pk_bf16_f32 v118, v34, v35
	ds_write2_b32 v130, v133, v118 offset0:136 offset1:204
	v_pk_mul_f32 v[36:37], v[42:43], v[36:37]
	v_lshlrev_b32_e32 v42, 16, v156
	v_and_b32_e32 v43, 0xffff0000, v156
	v_pk_mul_f32 v[38:39], v[38:39], v[42:43]
	v_cvt_pk_bf16_f32 v121, v36, v37
	v_cvt_pk_bf16_f32 v120, v38, v39
	v_add_f32_e32 v38, v114, v166
	v_add_f32_e32 v39, v115, v47
	v_exp_f32_e32 v38, v38
	v_exp_f32_e32 v39, v39
	v_mov_b32_e32 v43, v36
	v_mov_b32_e32 v36, v35
	v_pk_mul_f32 v[118:119], v[46:47], v[36:37] op_sel_hi:[0,1]
	v_lshlrev_b32_e32 v36, 16, v159
	v_and_b32_e32 v37, 0xffff0000, v159
	v_pk_mul_f32 v[36:37], v[38:39], v[36:37]
	v_rcp_f32_e32 v114, v38
	v_cvt_pk_bf16_f32 v38, v36, v37
	v_add_f32_e32 v36, v112, v166
	v_add_f32_e32 v37, v113, v47
	v_rcp_f32_e32 v115, v39
	v_exp_f32_e32 v36, v36
	v_exp_f32_e32 v37, v37
	v_add_u32_e32 v39, 0x400, v131
	v_mov_b32_e32 v42, v34
	v_pk_mul_f32 v[34:35], v[44:45], v[114:115]
	ds_write2_b32 v39, v120, v38 offset0:16 offset1:84
	v_rcp_f32_e32 v38, v36
	v_rcp_f32_e32 v39, v37
	v_cvt_pk_bf16_f32 v44, v34, v35
	v_add_u32_e32 v45, 0x4800, v131
	ds_write2_b32 v45, v121, v44 offset0:16 offset1:84
	v_lshlrev_b32_e32 v44, 16, v164
	v_and_b32_e32 v45, 0xffff0000, v164
	v_pk_add_f32 v[48:49], v[108:109], v[142:143] neg_lo:[0,1] neg_hi:[0,1]
	v_pk_mul_f32 v[36:37], v[36:37], v[44:45]
	v_pk_mul_f32 v[38:39], v[48:49], v[38:39]
	v_cvt_pk_bf16_f32 v36, v36, v37
	ds_write_b32 v131, v36 offset:1632
	v_cvt_pk_bf16_f32 v36, v38, v39
	ds_write_b32 v131, v36 offset:19040
	v_mov_b32_e32 v36, v34
	v_mov_b32_e32 v37, v38
	v_pk_mul_f32 v[122:123], v[116:117], v[122:123] op_sel_hi:[0,1]
	v_pk_mul_f32 v[124:125], v[116:117], v[124:125] op_sel_hi:[0,1]
	v_pk_mul_f32 v[42:43], v[116:117], v[42:43] op_sel_hi:[0,1]
	v_pk_mul_f32 v[44:45], v[116:117], v[36:37] op_sel_hi:[0,1]
	v_mov_b32_e32 v38, v35
	v_pk_mul_f32 v[38:39], v[46:47], v[38:39] op_sel_hi:[0,1]
	v_cvt_pk_bf16_f32 v34, v122, v123
	v_cvt_pk_bf16_f32 v35, v124, v125
	v_cvt_pk_bf16_f32 v36, v42, v43
	v_cvt_pk_bf16_f32 v37, v44, v45
	ds_write_b128 v204, v[34:37] offset:34816
	v_cvt_pk_bf16_f32 v34, v40, v41
	v_cvt_pk_bf16_f32 v35, v128, v129
	v_cvt_pk_bf16_f32 v36, v118, v119
	v_cvt_pk_bf16_f32 v37, v38, v39
	s_cmpk_eq_i32 s90, 0xffc0
	ds_write_b128 v204, v[34:37] offset:34960
	s_cbranch_scc1 .LBB0_363
	s_add_i32 s61, s89, 64
	s_and_b64 s[58:59], s[40:41], exec
	s_cselect_b32 s58, s61, s90
	s_add_i32 s58, s58, s88
	s_mul_hi_i32 s59, s58, 0x3800
	s_mulk_i32 s58, 0x3800
	s_add_u32 s58, s55, s58
	s_addc_u32 s59, s73, s59
	s_add_u32 s86, s58, s70
	s_addc_u32 s87, s59, 0
	s_add_u32 s84, s58, 0x1000
	s_addc_u32 s85, s59, 0
	s_add_u32 s82, s58, 0x2800
	v_lshl_add_u64 v[34:35], s[86:87], 0, v[68:69]
	s_addc_u32 s83, s59, 0
	global_load_dword v87, v[34:35], off
	v_lshl_add_u64 v[34:35], s[84:85], 0, v[68:69]
	global_load_dword v89, v[34:35], off
	v_lshl_add_u64 v[34:35], s[82:83], 0, v[68:69]
	global_load_dword v91, v[34:35], off
	v_lshl_add_u64 v[34:35], s[86:87], 0, v[52:53]
	global_load_dword v93, v[34:35], off
	v_lshl_add_u64 v[34:35], s[84:85], 0, v[52:53]
	global_load_dword v97, v[34:35], off
	v_lshl_add_u64 v[34:35], s[82:83], 0, v[52:53]
	global_load_dword v107, v[34:35], off
	v_lshl_add_u64 v[34:35], s[86:87], 0, v[54:55]
	global_load_dword v146, v[34:35], off
	v_lshl_add_u64 v[34:35], s[84:85], 0, v[54:55]
	global_load_dword v147, v[34:35], off
	v_lshl_add_u64 v[34:35], s[82:83], 0, v[54:55]
	global_load_dword v148, v[34:35], off
	v_lshl_add_u64 v[34:35], s[86:87], 0, v[56:57]
	global_load_dword v149, v[34:35], off
	v_lshl_add_u64 v[34:35], s[84:85], 0, v[56:57]
	global_load_dword v150, v[34:35], off
	v_lshl_add_u64 v[34:35], s[82:83], 0, v[56:57]
	global_load_dword v151, v[34:35], off
	v_lshl_add_u64 v[34:35], s[86:87], 0, v[58:59]
	global_load_dword v152, v[34:35], off
	v_lshl_add_u64 v[34:35], s[84:85], 0, v[58:59]
	global_load_dword v153, v[34:35], off
	v_lshl_add_u64 v[34:35], s[82:83], 0, v[58:59]
	global_load_dword v154, v[34:35], off
	v_lshl_add_u64 v[34:35], s[86:87], 0, v[60:61]
	global_load_dword v155, v[34:35], off
	v_lshl_add_u64 v[34:35], s[84:85], 0, v[60:61]
	global_load_dword v156, v[34:35], off
	v_lshl_add_u64 v[34:35], s[82:83], 0, v[60:61]
	global_load_dword v157, v[34:35], off
	v_lshl_add_u64 v[34:35], s[86:87], 0, v[62:63]
	global_load_dword v158, v[34:35], off
	v_lshl_add_u64 v[34:35], s[84:85], 0, v[62:63]
	global_load_dword v159, v[34:35], off
	v_lshl_add_u64 v[34:35], s[82:83], 0, v[62:63]
	global_load_dword v160, v[34:35], off
	v_lshl_add_u64 v[34:35], s[86:87], 0, v[50:51]
	global_load_dword v161, v[34:35], off
	v_lshl_add_u64 v[34:35], s[84:85], 0, v[50:51]
	global_load_dword v164, v[34:35], off
	v_lshl_add_u64 v[34:35], s[82:83], 0, v[50:51]
	global_load_dword v165, v[34:35], off
